# speedup vs baseline: 1.0064x; 1.0064x over previous
.Lsc_dskip15:
	s_waitcnt lgkmcnt(0)
	s_barrier
	v_lshlrev_b32_e32 v50, 3, v0
	v_mov_b32_e32 v52, 0
	v_mov_b32_e32 v53, 0
	v_cmp_gt_u32_e32 vcc, 0x224, v0
	s_and_saveexec_b64 s[36:37], vcc
	ds_read_b64 v[52:53], v50 offset:4608
	s_mov_b64 exec, s[36:37]
	s_waitcnt lgkmcnt(0)
	v_add_u32_e32 v54, v52, v53
	v_mov_b32_e32 v55, v54
	s_nop 1
	v_add_u32_dpp v55, v55, v55 row_shr:1 row_mask:0xf bank_mask:0xf bound_ctrl:0
	s_nop 1
	v_add_u32_dpp v55, v55, v55 row_shr:2 row_mask:0xf bank_mask:0xf bound_ctrl:0
	s_nop 1
	v_add_u32_dpp v55, v55, v55 row_shr:4 row_mask:0xf bank_mask:0xf bound_ctrl:0
	s_nop 1
	v_add_u32_dpp v55, v55, v55 row_shr:8 row_mask:0xf bank_mask:0xf bound_ctrl:0
	s_nop 1
	v_add_u32_dpp v55, v55, v55 row_bcast:15 row_mask:0xa bank_mask:0xf
	s_nop 1
	v_add_u32_dpp v55, v55, v55 row_bcast:31 row_mask:0xc bank_mask:0xf
	v_lshrrev_b32_e32 v56, 6, v0
	s_nop 0
	v_readfirstlane_b32 s3, v56
	v_readlane_b32 s14, v55, 63
	s_lshl_b32 s15, s3, 2
	s_add_u32 s15, s15, 0x2400
	v_mov_b32_e32 v57, s14
	v_mov_b32_e32 v58, s15
	s_mov_b64 s[38:39], exec
	s_mov_b64 exec, 1
	ds_write_b32 v58, v57
	s_mov_b64 exec, s[38:39]
	s_waitcnt lgkmcnt(0)
	s_barrier
	v_and_b32_e32 v57, 15, v0
	v_lshlrev_b32_e32 v57, 2, v57
	ds_read_b32 v57, v57 offset:9216
	s_waitcnt lgkmcnt(0)
	s_nop 1
	v_add_u32_dpp v57, v57, v57 row_shr:1 row_mask:0xf bank_mask:0xf bound_ctrl:0
	s_nop 1
	v_add_u32_dpp v57, v57, v57 row_shr:2 row_mask:0xf bank_mask:0xf bound_ctrl:0
	s_nop 1
	v_add_u32_dpp v57, v57, v57 row_shr:4 row_mask:0xf bank_mask:0xf bound_ctrl:0
	s_nop 1
	v_add_u32_dpp v57, v57, v57 row_shr:8 row_mask:0xf bank_mask:0xf bound_ctrl:0
	s_sub_u32 s15, s3, 1
	s_max_i32 s15, s15, 0
	s_nop 1
	v_readlane_b32 s16, v57, s15
	s_cmp_eq_u32 s3, 0
	s_cselect_b32 s16, 0, s16
	v_sub_u32_e32 v58, v55, v54
	v_add_u32_e32 v58, s16, v58
	v_add_u32_e32 v59, v58, v52
	v_cmp_gt_u32_e32 vcc, 0x224, v0
	s_and_saveexec_b64 s[36:37], vcc
	ds_read_b64 v[56:57], v50
	ds_write_b64 v50, v[58:59] offset:9728
	s_waitcnt lgkmcnt(0)
	v_sub_u32_e32 v56, v56, v58
	v_sub_u32_e32 v57, v57, v59
	ds_write_b64 v50, v[56:57]
	s_mov_b64 exec, s[36:37]
	s_waitcnt lgkmcnt(0)
	s_barrier
	v_mov_b32_e32 v60, 0x447
	v_cmp_gt_i32_e64 s[20:21], 0, v3
	v_subrev_co_u32_e32 v51, vcc, 0x61a80, v3
	v_lshrrev_b32_e32 v51, 6, v51
	v_lshrrev_b32_e32 v52, 9, v3
	v_add_u32_e32 v51, 0x30e, v51
	v_cndmask_b32_e32 v51, v51, v52, vcc
	v_cndmask_b32_e64 v51, v51, v60, s[20:21]
	v_lshlrev_b32_e32 v51, 2, v51
	ds_read_b32 v53, v51 offset:9728
	v_cmp_gt_i32_e64 s[20:21], 0, v5
	v_subrev_co_u32_e32 v51, vcc, 0x61a80, v5
	v_lshrrev_b32_e32 v51, 6, v51
	v_lshrrev_b32_e32 v52, 9, v5
	v_add_u32_e32 v51, 0x30e, v51
	v_cndmask_b32_e32 v51, v51, v52, vcc
	v_cndmask_b32_e64 v51, v51, v60, s[20:21]
	v_lshlrev_b32_e32 v51, 2, v51
	ds_read_b32 v54, v51 offset:9728
	v_cmp_gt_i32_e64 s[20:21], 0, v7
	v_subrev_co_u32_e32 v51, vcc, 0x61a80, v7
	v_lshrrev_b32_e32 v51, 6, v51
	v_lshrrev_b32_e32 v52, 9, v7
	v_add_u32_e32 v51, 0x30e, v51
	v_cndmask_b32_e32 v51, v51, v52, vcc
	v_cndmask_b32_e64 v51, v51, v60, s[20:21]
	v_lshlrev_b32_e32 v51, 2, v51
	ds_read_b32 v55, v51 offset:9728
	v_cmp_gt_i32_e64 s[20:21], 0, v9
	v_subrev_co_u32_e32 v51, vcc, 0x61a80, v9
	v_lshrrev_b32_e32 v51, 6, v51
	v_lshrrev_b32_e32 v52, 9, v9
	v_add_u32_e32 v51, 0x30e, v51
	v_cndmask_b32_e32 v51, v51, v52, vcc
	v_cndmask_b32_e64 v51, v51, v60, s[20:21]
	v_lshlrev_b32_e32 v51, 2, v51
	ds_read_b32 v56, v51 offset:9728
	s_waitcnt lgkmcnt(0)
	v_add_u32_e32 v34, v34, v53
	v_add_u32_e32 v35, v35, v54
	v_add_u32_e32 v36, v36, v55
	v_add_u32_e32 v37, v37, v56
	v_cmp_gt_i32_e64 s[20:21], 0, v11
	v_subrev_co_u32_e32 v51, vcc, 0x61a80, v11
	v_lshrrev_b32_e32 v51, 6, v51
	v_lshrrev_b32_e32 v52, 9, v11
	v_add_u32_e32 v51, 0x30e, v51
	v_cndmask_b32_e32 v51, v51, v52, vcc
	v_cndmask_b32_e64 v51, v51, v60, s[20:21]
	v_lshlrev_b32_e32 v51, 2, v51
	ds_read_b32 v53, v51 offset:9728
	v_cmp_gt_i32_e64 s[20:21], 0, v13
	v_subrev_co_u32_e32 v51, vcc, 0x61a80, v13
	v_lshrrev_b32_e32 v51, 6, v51
	v_lshrrev_b32_e32 v52, 9, v13
	v_add_u32_e32 v51, 0x30e, v51
	v_cndmask_b32_e32 v51, v51, v52, vcc
	v_cndmask_b32_e64 v51, v51, v60, s[20:21]
	v_lshlrev_b32_e32 v51, 2, v51
	ds_read_b32 v54, v51 offset:9728
	v_cmp_gt_i32_e64 s[20:21], 0, v15
	v_subrev_co_u32_e32 v51, vcc, 0x61a80, v15
	v_lshrrev_b32_e32 v51, 6, v51
	v_lshrrev_b32_e32 v52, 9, v15
	v_add_u32_e32 v51, 0x30e, v51
	v_cndmask_b32_e32 v51, v51, v52, vcc
	v_cndmask_b32_e64 v51, v51, v60, s[20:21]
	v_lshlrev_b32_e32 v51, 2, v51
	ds_read_b32 v55, v51 offset:9728
	v_cmp_gt_i32_e64 s[20:21], 0, v17
	v_subrev_co_u32_e32 v51, vcc, 0x61a80, v17
	v_lshrrev_b32_e32 v51, 6, v51
	v_lshrrev_b32_e32 v52, 9, v17
	v_add_u32_e32 v51, 0x30e, v51
	v_cndmask_b32_e32 v51, v51, v52, vcc
	v_cndmask_b32_e64 v51, v51, v60, s[20:21]
	v_lshlrev_b32_e32 v51, 2, v51
	ds_read_b32 v56, v51 offset:9728
	s_waitcnt lgkmcnt(0)
	v_add_u32_e32 v38, v38, v53
	v_add_u32_e32 v39, v39, v54
	v_add_u32_e32 v40, v40, v55
	v_add_u32_e32 v41, v41, v56
	v_cmp_gt_i32_e64 s[20:21], 0, v19
	v_subrev_co_u32_e32 v51, vcc, 0x61a80, v19
	v_lshrrev_b32_e32 v51, 6, v51
	v_lshrrev_b32_e32 v52, 9, v19
	v_add_u32_e32 v51, 0x30e, v51
	v_cndmask_b32_e32 v51, v51, v52, vcc
	v_cndmask_b32_e64 v51, v51, v60, s[20:21]
	v_lshlrev_b32_e32 v51, 2, v51
	ds_read_b32 v53, v51 offset:9728
	v_cmp_gt_i32_e64 s[20:21], 0, v21
	v_subrev_co_u32_e32 v51, vcc, 0x61a80, v21
	v_lshrrev_b32_e32 v51, 6, v51
	v_lshrrev_b32_e32 v52, 9, v21
	v_add_u32_e32 v51, 0x30e, v51
	v_cndmask_b32_e32 v51, v51, v52, vcc
	v_cndmask_b32_e64 v51, v51, v60, s[20:21]
	v_lshlrev_b32_e32 v51, 2, v51
	ds_read_b32 v54, v51 offset:9728
	v_cmp_gt_i32_e64 s[20:21], 0, v23
	v_subrev_co_u32_e32 v51, vcc, 0x61a80, v23
	v_lshrrev_b32_e32 v51, 6, v51
	v_lshrrev_b32_e32 v52, 9, v23
	v_add_u32_e32 v51, 0x30e, v51
	v_cndmask_b32_e32 v51, v51, v52, vcc
	v_cndmask_b32_e64 v51, v51, v60, s[20:21]
	v_lshlrev_b32_e32 v51, 2, v51
	ds_read_b32 v55, v51 offset:9728
	v_cmp_gt_i32_e64 s[20:21], 0, v25
	v_subrev_co_u32_e32 v51, vcc, 0x61a80, v25
	v_lshrrev_b32_e32 v51, 6, v51
	v_lshrrev_b32_e32 v52, 9, v25
	v_add_u32_e32 v51, 0x30e, v51
	v_cndmask_b32_e32 v51, v51, v52, vcc
	v_cndmask_b32_e64 v51, v51, v60, s[20:21]
	v_lshlrev_b32_e32 v51, 2, v51
	ds_read_b32 v56, v51 offset:9728
	s_waitcnt lgkmcnt(0)
	v_add_u32_e32 v42, v42, v53
	v_add_u32_e32 v43, v43, v54
	v_add_u32_e32 v44, v44, v55
	v_add_u32_e32 v45, v45, v56
	v_cmp_gt_i32_e64 s[20:21], 0, v27
	v_subrev_co_u32_e32 v51, vcc, 0x61a80, v27
	v_lshrrev_b32_e32 v51, 6, v51
	v_lshrrev_b32_e32 v52, 9, v27
	v_add_u32_e32 v51, 0x30e, v51
	v_cndmask_b32_e32 v51, v51, v52, vcc
	v_cndmask_b32_e64 v51, v51, v60, s[20:21]
	v_lshlrev_b32_e32 v51, 2, v51
	ds_read_b32 v53, v51 offset:9728
	v_cmp_gt_i32_e64 s[20:21], 0, v29
	v_subrev_co_u32_e32 v51, vcc, 0x61a80, v29
	v_lshrrev_b32_e32 v51, 6, v51
	v_lshrrev_b32_e32 v52, 9, v29
	v_add_u32_e32 v51, 0x30e, v51
	v_cndmask_b32_e32 v51, v51, v52, vcc
	v_cndmask_b32_e64 v51, v51, v60, s[20:21]
	v_lshlrev_b32_e32 v51, 2, v51
	ds_read_b32 v54, v51 offset:9728
	v_cmp_gt_i32_e64 s[20:21], 0, v31
	v_subrev_co_u32_e32 v51, vcc, 0x61a80, v31
	v_lshrrev_b32_e32 v51, 6, v51
	v_lshrrev_b32_e32 v52, 9, v31
	v_add_u32_e32 v51, 0x30e, v51
	v_cndmask_b32_e32 v51, v51, v52, vcc
	v_cndmask_b32_e64 v51, v51, v60, s[20:21]
	v_lshlrev_b32_e32 v51, 2, v51
	ds_read_b32 v55, v51 offset:9728
	v_cmp_gt_i32_e64 s[20:21], 0, v33
	v_subrev_co_u32_e32 v51, vcc, 0x61a80, v33
	v_lshrrev_b32_e32 v51, 6, v51
	v_lshrrev_b32_e32 v52, 9, v33
	v_add_u32_e32 v51, 0x30e, v51
	v_cndmask_b32_e32 v51, v51, v52, vcc
	v_cndmask_b32_e64 v51, v51, v60, s[20:21]
	v_lshlrev_b32_e32 v51, 2, v51
	ds_read_b32 v56, v51 offset:9728
	s_waitcnt lgkmcnt(0)
	v_add_u32_e32 v46, v46, v53
	v_add_u32_e32 v47, v47, v54
	v_add_u32_e32 v48, v48, v55
	v_add_u32_e32 v49, v49, v56
	s_mov_b64 s[38:39], exec
	s_movk_i32 s14, 0x4000
	v_cmp_gt_u32_e32 vcc, s14, v34
	v_lshlrev_b32_e32 v52, 3, v34
	s_and_b64 exec, s[38:39], vcc
	ds_write_b64 v52, v[2:3] offset:14336
	s_mov_b64 exec, s[38:39]
	v_cmp_gt_u32_e32 vcc, s14, v35
	v_lshlrev_b32_e32 v52, 3, v35
	s_and_b64 exec, s[38:39], vcc
	ds_write_b64 v52, v[4:5] offset:14336
	s_mov_b64 exec, s[38:39]
	v_cmp_gt_u32_e32 vcc, s14, v36
	v_lshlrev_b32_e32 v52, 3, v36
	s_and_b64 exec, s[38:39], vcc
	ds_write_b64 v52, v[6:7] offset:14336
	s_mov_b64 exec, s[38:39]
	v_cmp_gt_u32_e32 vcc, s14, v37
	v_lshlrev_b32_e32 v52, 3, v37
	s_and_b64 exec, s[38:39], vcc
	ds_write_b64 v52, v[8:9] offset:14336
	s_mov_b64 exec, s[38:39]
	v_cmp_gt_u32_e32 vcc, s14, v38
	v_lshlrev_b32_e32 v52, 3, v38
	s_and_b64 exec, s[38:39], vcc
	ds_write_b64 v52, v[10:11] offset:14336
	s_mov_b64 exec, s[38:39]
	v_cmp_gt_u32_e32 vcc, s14, v39
	v_lshlrev_b32_e32 v52, 3, v39
	s_and_b64 exec, s[38:39], vcc
	ds_write_b64 v52, v[12:13] offset:14336
	s_mov_b64 exec, s[38:39]
	v_cmp_gt_u32_e32 vcc, s14, v40
	v_lshlrev_b32_e32 v52, 3, v40
	s_and_b64 exec, s[38:39], vcc
	ds_write_b64 v52, v[14:15] offset:14336
	s_mov_b64 exec, s[38:39]
	v_cmp_gt_u32_e32 vcc, s14, v41
	v_lshlrev_b32_e32 v52, 3, v41
	s_and_b64 exec, s[38:39], vcc
	ds_write_b64 v52, v[16:17] offset:14336
	s_mov_b64 exec, s[38:39]
	v_cmp_gt_u32_e32 vcc, s14, v42
	v_lshlrev_b32_e32 v52, 3, v42
	s_and_b64 exec, s[38:39], vcc
	ds_write_b64 v52, v[18:19] offset:14336
	s_mov_b64 exec, s[38:39]
	v_cmp_gt_u32_e32 vcc, s14, v43
	v_lshlrev_b32_e32 v52, 3, v43
	s_and_b64 exec, s[38:39], vcc
	ds_write_b64 v52, v[20:21] offset:14336
	s_mov_b64 exec, s[38:39]
	v_cmp_gt_u32_e32 vcc, s14, v44
	v_lshlrev_b32_e32 v52, 3, v44
	s_and_b64 exec, s[38:39], vcc
	ds_write_b64 v52, v[22:23] offset:14336
	s_mov_b64 exec, s[38:39]
	v_cmp_gt_u32_e32 vcc, s14, v45
	v_lshlrev_b32_e32 v52, 3, v45
	s_and_b64 exec, s[38:39], vcc
	ds_write_b64 v52, v[24:25] offset:14336
	s_mov_b64 exec, s[38:39]
	v_cmp_gt_u32_e32 vcc, s14, v46
	v_lshlrev_b32_e32 v52, 3, v46
	s_and_b64 exec, s[38:39], vcc
	ds_write_b64 v52, v[26:27] offset:14336
	s_mov_b64 exec, s[38:39]
	v_cmp_gt_u32_e32 vcc, s14, v47
	v_lshlrev_b32_e32 v52, 3, v47
	s_and_b64 exec, s[38:39], vcc
	ds_write_b64 v52, v[28:29] offset:14336
	s_mov_b64 exec, s[38:39]
	v_cmp_gt_u32_e32 vcc, s14, v48
	v_lshlrev_b32_e32 v52, 3, v48
	s_and_b64 exec, s[38:39], vcc
	ds_write_b64 v52, v[30:31] offset:14336
	s_mov_b64 exec, s[38:39]
	v_cmp_gt_u32_e32 vcc, s14, v49
	v_lshlrev_b32_e32 v52, 3, v49
	s_and_b64 exec, s[38:39], vcc
	ds_write_b64 v52, v[32:33] offset:14336
	s_mov_b64 exec, s[38:39]
	s_waitcnt lgkmcnt(0)
	s_barrier
	v_mov_b32_e32 v61, v0
	v_lshlrev_b32_e32 v62, 3, v61
	ds_read_b64 v[50:51], v62 offset:14336
	s_waitcnt lgkmcnt(0)
	v_subrev_co_u32_e32 v53, vcc, 0x61a80, v51
	v_lshrrev_b32_e32 v53, 6, v53
	v_lshrrev_b32_e32 v54, 9, v51
	v_add_u32_e32 v53, 0x30e, v53
	v_cndmask_b32_e32 v53, v53, v54, vcc
	v_min_u32_e32 v53, 0x447, v53
	v_lshlrev_b32_e32 v53, 2, v53
	ds_read_b32 v53, v53
	v_cmp_le_i32_e32 vcc, 0, v51
	s_waitcnt lgkmcnt(0)
	v_add_u32_e32 v53, v53, v61
	v_lshlrev_b32_e32 v53, 3, v53
	s_and_b64 exec, s[38:39], vcc
	global_store_dwordx2 v53, v[50:51], s[34:35]
	s_mov_b64 exec, s[38:39]
	v_add_u32_e32 v61, 0x400, v0
	v_lshlrev_b32_e32 v62, 3, v61
	ds_read_b64 v[50:51], v62 offset:14336
	s_waitcnt lgkmcnt(0)
	v_subrev_co_u32_e32 v53, vcc, 0x61a80, v51
	v_lshrrev_b32_e32 v53, 6, v53
	v_lshrrev_b32_e32 v54, 9, v51
	v_add_u32_e32 v53, 0x30e, v53
	v_cndmask_b32_e32 v53, v53, v54, vcc
	v_min_u32_e32 v53, 0x447, v53
	v_lshlrev_b32_e32 v53, 2, v53
	ds_read_b32 v53, v53
	v_cmp_le_i32_e32 vcc, 0, v51
	s_waitcnt lgkmcnt(0)
	v_add_u32_e32 v53, v53, v61
	v_lshlrev_b32_e32 v53, 3, v53
	s_and_b64 exec, s[38:39], vcc
	global_store_dwordx2 v53, v[50:51], s[34:35]
	s_mov_b64 exec, s[38:39]
	v_add_u32_e32 v61, 0x800, v0
	v_lshlrev_b32_e32 v62, 3, v61
	ds_read_b64 v[50:51], v62 offset:14336
	s_waitcnt lgkmcnt(0)
	v_subrev_co_u32_e32 v53, vcc, 0x61a80, v51
	v_lshrrev_b32_e32 v53, 6, v53
	v_lshrrev_b32_e32 v54, 9, v51
	v_add_u32_e32 v53, 0x30e, v53
	v_cndmask_b32_e32 v53, v53, v54, vcc
	v_min_u32_e32 v53, 0x447, v53
	v_lshlrev_b32_e32 v53, 2, v53
	ds_read_b32 v53, v53
	v_cmp_le_i32_e32 vcc, 0, v51
	s_waitcnt lgkmcnt(0)
	v_add_u32_e32 v53, v53, v61
	v_lshlrev_b32_e32 v53, 3, v53
	s_and_b64 exec, s[38:39], vcc
	global_store_dwordx2 v53, v[50:51], s[34:35]
	s_mov_b64 exec, s[38:39]
	v_add_u32_e32 v61, 0xc00, v0
	v_lshlrev_b32_e32 v62, 3, v61
	ds_read_b64 v[50:51], v62 offset:14336
	s_waitcnt lgkmcnt(0)
	v_subrev_co_u32_e32 v53, vcc, 0x61a80, v51
	v_lshrrev_b32_e32 v53, 6, v53
	v_lshrrev_b32_e32 v54, 9, v51
	v_add_u32_e32 v53, 0x30e, v53
	v_cndmask_b32_e32 v53, v53, v54, vcc
	v_min_u32_e32 v53, 0x447, v53
	v_lshlrev_b32_e32 v53, 2, v53
	ds_read_b32 v53, v53
	v_cmp_le_i32_e32 vcc, 0, v51
	s_waitcnt lgkmcnt(0)
	v_add_u32_e32 v53, v53, v61
	v_lshlrev_b32_e32 v53, 3, v53
	s_and_b64 exec, s[38:39], vcc
	global_store_dwordx2 v53, v[50:51], s[34:35]
	s_mov_b64 exec, s[38:39]
	v_add_u32_e32 v61, 0x1000, v0
	v_lshlrev_b32_e32 v62, 3, v61
	ds_read_b64 v[50:51], v62 offset:14336
	s_waitcnt lgkmcnt(0)
	v_subrev_co_u32_e32 v53, vcc, 0x61a80, v51
	v_lshrrev_b32_e32 v53, 6, v53
	v_lshrrev_b32_e32 v54, 9, v51
	v_add_u32_e32 v53, 0x30e, v53
	v_cndmask_b32_e32 v53, v53, v54, vcc
	v_min_u32_e32 v53, 0x447, v53
	v_lshlrev_b32_e32 v53, 2, v53
	ds_read_b32 v53, v53
	v_cmp_le_i32_e32 vcc, 0, v51
	s_waitcnt lgkmcnt(0)
	v_add_u32_e32 v53, v53, v61
	v_lshlrev_b32_e32 v53, 3, v53
	s_and_b64 exec, s[38:39], vcc
	global_store_dwordx2 v53, v[50:51], s[34:35]
	s_mov_b64 exec, s[38:39]
	v_add_u32_e32 v61, 0x1400, v0
	v_lshlrev_b32_e32 v62, 3, v61
	ds_read_b64 v[50:51], v62 offset:14336
	s_waitcnt lgkmcnt(0)
	v_subrev_co_u32_e32 v53, vcc, 0x61a80, v51
	v_lshrrev_b32_e32 v53, 6, v53
	v_lshrrev_b32_e32 v54, 9, v51
	v_add_u32_e32 v53, 0x30e, v53
	v_cndmask_b32_e32 v53, v53, v54, vcc
	v_min_u32_e32 v53, 0x447, v53
	v_lshlrev_b32_e32 v53, 2, v53
	ds_read_b32 v53, v53
	v_cmp_le_i32_e32 vcc, 0, v51
	s_waitcnt lgkmcnt(0)
	v_add_u32_e32 v53, v53, v61
	v_lshlrev_b32_e32 v53, 3, v53
	s_and_b64 exec, s[38:39], vcc
	global_store_dwordx2 v53, v[50:51], s[34:35]
	s_mov_b64 exec, s[38:39]
	v_add_u32_e32 v61, 0x1800, v0
	v_lshlrev_b32_e32 v62, 3, v61
	ds_read_b64 v[50:51], v62 offset:14336
	s_waitcnt lgkmcnt(0)
	v_subrev_co_u32_e32 v53, vcc, 0x61a80, v51
	v_lshrrev_b32_e32 v53, 6, v53
	v_lshrrev_b32_e32 v54, 9, v51
	v_add_u32_e32 v53, 0x30e, v53
	v_cndmask_b32_e32 v53, v53, v54, vcc
	v_min_u32_e32 v53, 0x447, v53
	v_lshlrev_b32_e32 v53, 2, v53
	ds_read_b32 v53, v53
	v_cmp_le_i32_e32 vcc, 0, v51
	s_waitcnt lgkmcnt(0)
	v_add_u32_e32 v53, v53, v61
	v_lshlrev_b32_e32 v53, 3, v53
	s_and_b64 exec, s[38:39], vcc
	global_store_dwordx2 v53, v[50:51], s[34:35]
	s_mov_b64 exec, s[38:39]
	v_add_u32_e32 v61, 0x1c00, v0
	v_lshlrev_b32_e32 v62, 3, v61
	ds_read_b64 v[50:51], v62 offset:14336
	s_waitcnt lgkmcnt(0)
	v_subrev_co_u32_e32 v53, vcc, 0x61a80, v51
	v_lshrrev_b32_e32 v53, 6, v53
	v_lshrrev_b32_e32 v54, 9, v51
	v_add_u32_e32 v53, 0x30e, v53
	v_cndmask_b32_e32 v53, v53, v54, vcc
	v_min_u32_e32 v53, 0x447, v53
	v_lshlrev_b32_e32 v53, 2, v53
	ds_read_b32 v53, v53
	v_cmp_le_i32_e32 vcc, 0, v51
	s_waitcnt lgkmcnt(0)
	v_add_u32_e32 v53, v53, v61
	v_lshlrev_b32_e32 v53, 3, v53
	s_and_b64 exec, s[38:39], vcc
	global_store_dwordx2 v53, v[50:51], s[34:35]
	s_mov_b64 exec, s[38:39]
	v_add_u32_e32 v61, 0x2000, v0
	v_lshlrev_b32_e32 v62, 3, v61
	ds_read_b64 v[50:51], v62 offset:14336
	s_waitcnt lgkmcnt(0)
	v_subrev_co_u32_e32 v53, vcc, 0x61a80, v51
	v_lshrrev_b32_e32 v53, 6, v53
	v_lshrrev_b32_e32 v54, 9, v51
	v_add_u32_e32 v53, 0x30e, v53
	v_cndmask_b32_e32 v53, v53, v54, vcc
	v_min_u32_e32 v53, 0x447, v53
	v_lshlrev_b32_e32 v53, 2, v53
	ds_read_b32 v53, v53
	v_cmp_le_i32_e32 vcc, 0, v51
	s_waitcnt lgkmcnt(0)
	v_add_u32_e32 v53, v53, v61
	v_lshlrev_b32_e32 v53, 3, v53
	s_and_b64 exec, s[38:39], vcc
	global_store_dwordx2 v53, v[50:51], s[34:35]
	s_mov_b64 exec, s[38:39]
	v_add_u32_e32 v61, 0x2400, v0
	v_lshlrev_b32_e32 v62, 3, v61
	ds_read_b64 v[50:51], v62 offset:14336
	s_waitcnt lgkmcnt(0)
	v_subrev_co_u32_e32 v53, vcc, 0x61a80, v51
	v_lshrrev_b32_e32 v53, 6, v53
	v_lshrrev_b32_e32 v54, 9, v51
	v_add_u32_e32 v53, 0x30e, v53
	v_cndmask_b32_e32 v53, v53, v54, vcc
	v_min_u32_e32 v53, 0x447, v53
	v_lshlrev_b32_e32 v53, 2, v53
	ds_read_b32 v53, v53
	v_cmp_le_i32_e32 vcc, 0, v51
	s_waitcnt lgkmcnt(0)
	v_add_u32_e32 v53, v53, v61
	v_lshlrev_b32_e32 v53, 3, v53
	s_and_b64 exec, s[38:39], vcc
	global_store_dwordx2 v53, v[50:51], s[34:35]
	s_mov_b64 exec, s[38:39]
	v_add_u32_e32 v61, 0x2800, v0
	v_lshlrev_b32_e32 v62, 3, v61
	ds_read_b64 v[50:51], v62 offset:14336
	s_waitcnt lgkmcnt(0)
	v_subrev_co_u32_e32 v53, vcc, 0x61a80, v51
	v_lshrrev_b32_e32 v53, 6, v53
	v_lshrrev_b32_e32 v54, 9, v51
	v_add_u32_e32 v53, 0x30e, v53
	v_cndmask_b32_e32 v53, v53, v54, vcc
	v_min_u32_e32 v53, 0x447, v53
	v_lshlrev_b32_e32 v53, 2, v53
	ds_read_b32 v53, v53
	v_cmp_le_i32_e32 vcc, 0, v51
	s_waitcnt lgkmcnt(0)
	v_add_u32_e32 v53, v53, v61
	v_lshlrev_b32_e32 v53, 3, v53
	s_and_b64 exec, s[38:39], vcc
	global_store_dwordx2 v53, v[50:51], s[34:35]
	s_mov_b64 exec, s[38:39]
	v_add_u32_e32 v61, 0x2c00, v0
	v_lshlrev_b32_e32 v62, 3, v61
	ds_read_b64 v[50:51], v62 offset:14336
	s_waitcnt lgkmcnt(0)
	v_subrev_co_u32_e32 v53, vcc, 0x61a80, v51
	v_lshrrev_b32_e32 v53, 6, v53
	v_lshrrev_b32_e32 v54, 9, v51
	v_add_u32_e32 v53, 0x30e, v53
	v_cndmask_b32_e32 v53, v53, v54, vcc
	v_min_u32_e32 v53, 0x447, v53
	v_lshlrev_b32_e32 v53, 2, v53
	ds_read_b32 v53, v53
	v_cmp_le_i32_e32 vcc, 0, v51
	s_waitcnt lgkmcnt(0)
	v_add_u32_e32 v53, v53, v61
	v_lshlrev_b32_e32 v53, 3, v53
	s_and_b64 exec, s[38:39], vcc
	global_store_dwordx2 v53, v[50:51], s[34:35]
	s_mov_b64 exec, s[38:39]
	v_add_u32_e32 v61, 0x3000, v0
	v_lshlrev_b32_e32 v62, 3, v61
	ds_read_b64 v[50:51], v62 offset:14336
	s_waitcnt lgkmcnt(0)
	v_subrev_co_u32_e32 v53, vcc, 0x61a80, v51
	v_lshrrev_b32_e32 v53, 6, v53
	v_lshrrev_b32_e32 v54, 9, v51
	v_add_u32_e32 v53, 0x30e, v53
	v_cndmask_b32_e32 v53, v53, v54, vcc
	v_min_u32_e32 v53, 0x447, v53
	v_lshlrev_b32_e32 v53, 2, v53
	ds_read_b32 v53, v53
	v_cmp_le_i32_e32 vcc, 0, v51
	s_waitcnt lgkmcnt(0)
	v_add_u32_e32 v53, v53, v61
	v_lshlrev_b32_e32 v53, 3, v53
	s_and_b64 exec, s[38:39], vcc
	global_store_dwordx2 v53, v[50:51], s[34:35]
	s_mov_b64 exec, s[38:39]
	v_add_u32_e32 v61, 0x3400, v0
	v_lshlrev_b32_e32 v62, 3, v61
	ds_read_b64 v[50:51], v62 offset:14336
	s_waitcnt lgkmcnt(0)
	v_subrev_co_u32_e32 v53, vcc, 0x61a80, v51
	v_lshrrev_b32_e32 v53, 6, v53
	v_lshrrev_b32_e32 v54, 9, v51
	v_add_u32_e32 v53, 0x30e, v53
	v_cndmask_b32_e32 v53, v53, v54, vcc
	v_min_u32_e32 v53, 0x447, v53
	v_lshlrev_b32_e32 v53, 2, v53
	ds_read_b32 v53, v53
	v_cmp_le_i32_e32 vcc, 0, v51
	s_waitcnt lgkmcnt(0)
	v_add_u32_e32 v53, v53, v61
	v_lshlrev_b32_e32 v53, 3, v53
	s_and_b64 exec, s[38:39], vcc
	global_store_dwordx2 v53, v[50:51], s[34:35]
	s_mov_b64 exec, s[38:39]
	v_add_u32_e32 v61, 0x3800, v0
	v_lshlrev_b32_e32 v62, 3, v61
	ds_read_b64 v[50:51], v62 offset:14336
	s_waitcnt lgkmcnt(0)
	v_subrev_co_u32_e32 v53, vcc, 0x61a80, v51
	v_lshrrev_b32_e32 v53, 6, v53
	v_lshrrev_b32_e32 v54, 9, v51
	v_add_u32_e32 v53, 0x30e, v53
	v_cndmask_b32_e32 v53, v53, v54, vcc
	v_min_u32_e32 v53, 0x447, v53
	v_lshlrev_b32_e32 v53, 2, v53
	ds_read_b32 v53, v53
	v_cmp_le_i32_e32 vcc, 0, v51
	s_waitcnt lgkmcnt(0)
	v_add_u32_e32 v53, v53, v61
	v_lshlrev_b32_e32 v53, 3, v53
	s_and_b64 exec, s[38:39], vcc
	global_store_dwordx2 v53, v[50:51], s[34:35]
	s_mov_b64 exec, s[38:39]
	v_add_u32_e32 v61, 0x3c00, v0
	v_lshlrev_b32_e32 v62, 3, v61
	ds_read_b64 v[50:51], v62 offset:14336
	s_waitcnt lgkmcnt(0)
	v_subrev_co_u32_e32 v53, vcc, 0x61a80, v51
	v_lshrrev_b32_e32 v53, 6, v53
	v_lshrrev_b32_e32 v54, 9, v51
	v_add_u32_e32 v53, 0x30e, v53
	v_cndmask_b32_e32 v53, v53, v54, vcc
	v_min_u32_e32 v53, 0x447, v53
	v_lshlrev_b32_e32 v53, 2, v53
	ds_read_b32 v53, v53
	v_cmp_le_i32_e32 vcc, 0, v51
	s_waitcnt lgkmcnt(0)
	v_add_u32_e32 v53, v53, v61
	v_lshlrev_b32_e32 v53, 3, v53
	s_and_b64 exec, s[38:39], vcc
	global_store_dwordx2 v53, v[50:51], s[34:35]
	s_mov_b64 exec, s[38:39]
	s_endpgm

	.amdhsa_kernel _Z6k_prepPKiS0_S0_S0_PiP15HIP_vector_typeIiLj2EEPKfS6_S0_S0_S0_S6_S6_S6_PDF16_S7_6WSpecs
		.amdhsa_group_segment_fixed_size 145408
		.amdhsa_private_segment_fixed_size 0
		.amdhsa_kernarg_size 616
		.amdhsa_user_sgpr_count 2
		.amdhsa_user_sgpr_dispatch_ptr 0
		.amdhsa_user_sgpr_queue_ptr 0
		.amdhsa_user_sgpr_kernarg_segment_ptr 1
		.amdhsa_user_sgpr_dispatch_id 0
		.amdhsa_user_sgpr_kernarg_preload_length 0
		.amdhsa_user_sgpr_kernarg_preload_offset 0
		.amdhsa_user_sgpr_private_segment_size 0
		.amdhsa_uses_dynamic_stack 0
		.amdhsa_enable_private_segment 0
		.amdhsa_system_sgpr_workgroup_id_x 1
		.amdhsa_system_sgpr_workgroup_id_y 0
		.amdhsa_system_sgpr_workgroup_id_z 0
		.amdhsa_system_sgpr_workgroup_info 0
		.amdhsa_system_vgpr_workitem_id 0
		.amdhsa_next_free_vgpr 88
		.amdhsa_next_free_sgpr 40
		.amdhsa_accum_offset 88
		.amdhsa_reserve_vcc 1
		.amdhsa_float_round_mode_32 0
		.amdhsa_float_round_mode_16_64 0
		.amdhsa_float_denorm_mode_32 3
		.amdhsa_float_denorm_mode_16_64 3
		.amdhsa_dx10_clamp 1
		.amdhsa_ieee_mode 1
		.amdhsa_fp16_overflow 0
		.amdhsa_tg_split 0
		.amdhsa_exception_fp_ieee_invalid_op 0
		.amdhsa_exception_fp_denorm_src 0
		.amdhsa_exception_fp_ieee_div_zero 0
		.amdhsa_exception_fp_ieee_overflow 0
		.amdhsa_exception_fp_ieee_underflow 0
		.amdhsa_exception_fp_ieee_inexact 0
		.amdhsa_exception_int_div_zero 0
	.end_amdhsa_kernel

amdhsa.kernels:
  - .agpr_count:     0
    .args:
      - .actual_access:  read_only
        .address_space:  global
        .offset:         0
        .size:           8
        .value_kind:     global_buffer
      - .actual_access:  read_only
        .address_space:  global
        .offset:         8
        .size:           8
        .value_kind:     global_buffer
      - .actual_access:  write_only
        .address_space:  global
        .offset:         16
        .size:           8
        .value_kind:     global_buffer
      - .address_space:  global
        .offset:         24
        .size:           8
        .value_kind:     global_buffer
    .group_segment_fixed_size: 20736
    .kernarg_segment_align: 8
    .kernarg_segment_size: 32
    .language:       OpenCL C
    .language_version:
      - 2
      - 0
    .max_flat_workgroup_size: 256
    .name:           _Z6k_bcsrPK15HIP_vector_typeIiLj2EEPKiPiS5_
    .private_segment_fixed_size: 0
    .sgpr_count:     40
    .sgpr_spill_count: 0
    .symbol:         _Z6k_bcsrPK15HIP_vector_typeIiLj2EEPKiPiS5_.kd
    .uniform_work_group_size: 1
    .uses_dynamic_stack: false
    .vgpr_count:     64
    .vgpr_spill_count: 0
    .wavefront_size: 64
  - .agpr_count:     0
    .args:
      - .actual_access:  read_only
        .address_space:  global
        .offset:         0
        .size:           8
        .value_kind:     global_buffer
      - .actual_access:  read_only
        .address_space:  global
        .offset:         8
        .size:           8
        .value_kind:     global_buffer
      - .actual_access:  read_only
        .address_space:  global
        .offset:         16
        .size:           8
        .value_kind:     global_buffer
      - .actual_access:  write_only
        .address_space:  global
        .offset:         24
        .size:           8
        .value_kind:     global_buffer
      - .actual_access:  write_only
        .address_space:  global
        .offset:         32
        .size:           8
        .value_kind:     global_buffer
      - .actual_access:  read_only
        .address_space:  global
        .offset:         40
        .size:           8
        .value_kind:     global_buffer
      - .actual_access:  read_only
        .address_space:  global
        .offset:         48
        .size:           8
        .value_kind:     global_buffer
      - .actual_access:  read_only
        .address_space:  global
        .offset:         56
        .size:           8
        .value_kind:     global_buffer
      - .actual_access:  read_only
        .address_space:  global
        .offset:         64
        .size:           8
        .value_kind:     global_buffer
      - .actual_access:  read_only
        .address_space:  global
        .offset:         72
        .size:           8
        .value_kind:     global_buffer
      - .actual_access:  read_only
        .address_space:  global
        .offset:         80
        .size:           8
        .value_kind:     global_buffer
      - .actual_access:  read_only
        .address_space:  global
        .offset:         88
        .size:           8
        .value_kind:     global_buffer
      - .actual_access:  read_only
        .address_space:  global
        .offset:         96
        .size:           8
        .value_kind:     global_buffer
      - .address_space:  global
        .offset:         104
        .size:           8
        .value_kind:     global_buffer
      - .address_space:  global
        .offset:         112
        .size:           8
        .value_kind:     global_buffer
    .group_segment_fixed_size: 4384
    .kernarg_segment_align: 8
    .kernarg_segment_size: 120
    .language:       OpenCL C
    .language_version:
      - 2
      - 0
    .max_flat_workgroup_size: 1024
    .name:           _Z8k_bcountPKiS0_S0_PiPjPKfS4_S0_S0_S0_S4_S4_S4_PDF16_S5_
    .private_segment_fixed_size: 0
    .sgpr_count:     26
    .sgpr_spill_count: 0
    .symbol:         _Z8k_bcountPKiS0_S0_PiPjPKfS4_S0_S0_S0_S4_S4_S4_PDF16_S5_.kd
    .uniform_work_group_size: 1
    .uses_dynamic_stack: false
    .vgpr_count:     41
    .vgpr_spill_count: 0
    .wavefront_size: 64
  - .agpr_count:     0
    .args:
      - .actual_access:  read_only
        .address_space:  global
        .offset:         0
        .size:           8
        .value_kind:     global_buffer
      - .actual_access:  read_only
        .address_space:  global
        .offset:         8
        .size:           8
        .value_kind:     global_buffer
      - .actual_access:  read_only
        .address_space:  global
        .offset:         16
        .size:           8
        .value_kind:     global_buffer
      - .actual_access:  read_only
        .address_space:  global
        .offset:         24
        .size:           8
        .value_kind:     global_buffer
      - .actual_access:  write_only
        .address_space:  global
        .offset:         32
        .size:           8
        .value_kind:     global_buffer
      - .actual_access:  write_only
        .address_space:  global
        .offset:         40
        .size:           8
        .value_kind:     global_buffer
      - .actual_access:  read_only
        .address_space:  global
        .offset:         48
        .size:           8
        .value_kind:     global_buffer
      - .actual_access:  read_only
        .address_space:  global
        .offset:         56
        .size:           8
        .value_kind:     global_buffer
      - .actual_access:  read_only
        .address_space:  global
        .offset:         64
        .size:           8
        .value_kind:     global_buffer
      - .actual_access:  read_only
        .address_space:  global
        .offset:         72
        .size:           8
        .value_kind:     global_buffer
      - .actual_access:  read_only
        .address_space:  global
        .offset:         80
        .size:           8
        .value_kind:     global_buffer
      - .actual_access:  read_only
        .address_space:  global
        .offset:         88
        .size:           8
        .value_kind:     global_buffer
      - .actual_access:  read_only
        .address_space:  global
        .offset:         96
        .size:           8
        .value_kind:     global_buffer
      - .actual_access:  read_only
        .address_space:  global
        .offset:         104
        .size:           8
        .value_kind:     global_buffer
      - .address_space:  global
        .offset:         112
        .size:           8
        .value_kind:     global_buffer
      - .address_space:  global
        .offset:         120
        .size:           8
        .value_kind:     global_buffer
      - .offset:         128
        .size:           488
        .value_kind:     by_value
    .group_segment_fixed_size: 145408
    .kernarg_segment_align: 8
    .kernarg_segment_size: 616
    .language:       OpenCL C
    .language_version:
      - 2
      - 0
    .max_flat_workgroup_size: 1024
    .name:           _Z6k_prepPKiS0_S0_S0_PiP15HIP_vector_typeIiLj2EEPKfS6_S0_S0_S0_S6_S6_S6_PDF16_S7_6WSpecs
    .private_segment_fixed_size: 0
    .sgpr_count:     44
    .sgpr_spill_count: 0
    .symbol:         _Z6k_prepPKiS0_S0_S0_PiP15HIP_vector_typeIiLj2EEPKfS6_S0_S0_S0_S6_S6_S6_PDF16_S7_6WSpecs.kd
    .uniform_work_group_size: 1
    .uses_dynamic_stack: false
    .vgpr_count:     88
    .vgpr_spill_count: 0
    .wavefront_size: 64
  - .agpr_count:     0
    .args:
      - .offset:         0
        .size:           104
        .value_kind:     by_value
      - .offset:         104
        .size:           4
        .value_kind:     hidden_block_count_x
      - .offset:         108
        .size:           4
        .value_kind:     hidden_block_count_y
      - .offset:         112
        .size:           4
        .value_kind:     hidden_block_count_z
      - .offset:         116
        .size:           2
        .value_kind:     hidden_group_size_x
      - .offset:         118
        .size:           2
        .value_kind:     hidden_group_size_y
      - .offset:         120
        .size:           2
        .value_kind:     hidden_group_size_z
      - .offset:         122
        .size:           2
        .value_kind:     hidden_remainder_x
      - .offset:         124
        .size:           2
        .value_kind:     hidden_remainder_y
      - .offset:         126
        .size:           2
        .value_kind:     hidden_remainder_z
      - .offset:         144
        .size:           8
        .value_kind:     hidden_global_offset_x
      - .offset:         152
        .size:           8
        .value_kind:     hidden_global_offset_y
      - .offset:         160
        .size:           8
        .value_kind:     hidden_global_offset_z
      - .offset:         168
        .size:           2
        .value_kind:     hidden_grid_dims
    .group_segment_fixed_size: 155140
    .kernarg_segment_align: 8
    .kernarg_segment_size: 360
    .language:       OpenCL C
    .language_version:
      - 2
      - 0
    .max_flat_workgroup_size: 768
    .name:           _Z12k_layer_pool9LayerArgs
    .private_segment_fixed_size: 0
    .sgpr_count:     50
    .sgpr_spill_count: 0
    .symbol:         _Z12k_layer_pool9LayerArgs.kd
    .uniform_work_group_size: 1
    .uses_dynamic_stack: false
    .vgpr_count:     168
    .vgpr_spill_count: 0
    .wavefront_size: 64
  - .agpr_count:     0
    .args:
      - .actual_access:  read_only
        .address_space:  global
        .offset:         0
        .size:           8
        .value_kind:     global_buffer
      - .actual_access:  read_only
        .address_space:  global
        .offset:         8
        .size:           8
        .value_kind:     global_buffer
      - .actual_access:  read_only
        .address_space:  global
        .offset:         16
        .size:           8
        .value_kind:     global_buffer
      - .actual_access:  read_only
        .address_space:  global
        .offset:         24
        .size:           8
        .value_kind:     global_buffer
      - .actual_access:  read_only
        .address_space:  global
        .offset:         32
        .size:           8
        .value_kind:     global_buffer
      - .actual_access:  read_only
        .address_space:  global
        .offset:         40
        .size:           8
        .value_kind:     global_buffer
      - .actual_access:  read_only
        .address_space:  global
        .offset:         48
        .size:           8
        .value_kind:     global_buffer
      - .actual_access:  write_only
        .address_space:  global
        .offset:         56
        .size:           8
        .value_kind:     global_buffer
    .group_segment_fixed_size: 2560
    .kernarg_segment_align: 8
    .kernarg_segment_size: 64
    .language:       OpenCL C
    .language_version:
      - 2
      - 0
    .max_flat_workgroup_size: 512
    .name:           _Z5k_mlpPKjPKfS2_S2_S2_S2_S2_Pf
    .private_segment_fixed_size: 0
    .sgpr_count:     18
    .sgpr_spill_count: 0
    .symbol:         _Z5k_mlpPKjPKfS2_S2_S2_S2_S2_Pf.kd
    .uniform_work_group_size: 1
    .uses_dynamic_stack: false
    .vgpr_count:     120
    .vgpr_spill_count: 0
    .wavefront_size: 64
  - .agpr_count:     0
    .args:
      - .offset:         0
        .size:           104
        .value_kind:     by_value
      - .offset:         104
        .size:           104
        .value_kind:     by_value
      - .offset:         208
        .size:           4
        .value_kind:     by_value
      - .offset:         216
        .size:           4
        .value_kind:     hidden_block_count_x
      - .offset:         220
        .size:           4
        .value_kind:     hidden_block_count_y
      - .offset:         224
        .size:           4
        .value_kind:     hidden_block_count_z
      - .offset:         228
        .size:           2
        .value_kind:     hidden_group_size_x
      - .offset:         230
        .size:           2
        .value_kind:     hidden_group_size_y
      - .offset:         232
        .size:           2
        .value_kind:     hidden_group_size_z
      - .offset:         234
        .size:           2
        .value_kind:     hidden_remainder_x
      - .offset:         236
        .size:           2
        .value_kind:     hidden_remainder_y
      - .offset:         238
        .size:           2
        .value_kind:     hidden_remainder_z
      - .offset:         256
        .size:           8
        .value_kind:     hidden_global_offset_x
      - .offset:         264
        .size:           8
        .value_kind:     hidden_global_offset_y
      - .offset:         272
        .size:           8
        .value_kind:     hidden_global_offset_z
      - .offset:         280
        .size:           2
        .value_kind:     hidden_grid_dims
    .group_segment_fixed_size: 151044
    .kernarg_segment_align: 8
    .kernarg_segment_size: 472
    .language:       OpenCL C
    .language_version:
      - 2
      - 0
    .max_flat_workgroup_size: 768
    .name:           _Z10k_layer_fhILi96ELb1EEv9LayerArgsS0_i
    .private_segment_fixed_size: 0
    .sgpr_count:     52
    .sgpr_spill_count: 0
    .symbol:         _Z10k_layer_fhILi96ELb1EEv9LayerArgsS0_i.kd
    .uniform_work_group_size: 1
    .uses_dynamic_stack: false
    .vgpr_count:     168
    .vgpr_spill_count: 0
    .wavefront_size: 64
  - .agpr_count:     0
    .args:
      - .offset:         0
        .size:           104
        .value_kind:     by_value
      - .offset:         104
        .size:           104
        .value_kind:     by_value
      - .offset:         208
        .size:           4
        .value_kind:     by_value
      - .offset:         216
        .size:           4
        .value_kind:     hidden_block_count_x
      - .offset:         220
        .size:           4
        .value_kind:     hidden_block_count_y
      - .offset:         224
        .size:           4
        .value_kind:     hidden_block_count_z
      - .offset:         228
        .size:           2
        .value_kind:     hidden_group_size_x
      - .offset:         230
        .size:           2
        .value_kind:     hidden_group_size_y
      - .offset:         232
        .size:           2
        .value_kind:     hidden_group_size_z
      - .offset:         234
        .size:           2
        .value_kind:     hidden_remainder_x
      - .offset:         236
        .size:           2
        .value_kind:     hidden_remainder_y
      - .offset:         238
        .size:           2
        .value_kind:     hidden_remainder_z
      - .offset:         256
        .size:           8
        .value_kind:     hidden_global_offset_x
      - .offset:         264
        .size:           8
        .value_kind:     hidden_global_offset_y
      - .offset:         272
        .size:           8
        .value_kind:     hidden_global_offset_z
      - .offset:         280
        .size:           2
        .value_kind:     hidden_grid_dims
    .group_segment_fixed_size: 151044
    .kernarg_segment_align: 8
    .kernarg_segment_size: 472
    .language:       OpenCL C
    .language_version:
      - 2
      - 0
    .max_flat_workgroup_size: 768
    .name:           _Z10k_layer_fhILi128ELb1EEv9LayerArgsS0_i
    .private_segment_fixed_size: 0
    .sgpr_count:     45
    .sgpr_spill_count: 0
    .symbol:         _Z10k_layer_fhILi128ELb1EEv9LayerArgsS0_i.kd
    .uniform_work_group_size: 1
    .uses_dynamic_stack: false
    .vgpr_count:     168
    .vgpr_spill_count: 0
    .wavefront_size: 64
